# k_agg1: dropped the s_nop 0 pads between back-to-back gather loads (xnack replay rule only)
# speedup vs baseline: 1.0132x; 1.0132x over previous
.Lagg_full:
	global_load_dwordx4 v[30:33], v[2:3], off
	v_add_u32_e32 v0, 8, v0
	v_cmp_ge_i32_e64 s[18:19], v0, v1
	v_lshl_add_u64 v[2:3], v[2:3], 0, 16
	s_or_b64 s[30:31], s[18:19], s[30:31]
	s_waitcnt vmcnt(0)
	v_mad_u32_u16 v39, v30, s34, v6
	v_mad_u32_u16 v38, v30, s34, v6 op_sel:[1,0,0,0]
	v_mad_u32_u16 v40, v31, s34, v6
	v_mad_u32_u16 v42, v31, s34, v6 op_sel:[1,0,0,0]
	v_mad_u32_u16 v46, v32, s34, v6
	v_mad_u32_u16 v50, v32, s34, v6 op_sel:[1,0,0,0]
	v_mad_u32_u16 v54, v33, s34, v6
	v_mad_u32_u16 v58, v33, s34, v6 op_sel:[1,0,0,0]
	global_load_dwordx4 v[30:33], v39, s[20:21]
	global_load_dwordx4 v[34:37], v38, s[20:21]
	s_nop 0
	global_load_dwordx4 v[38:41], v40, s[20:21]
	global_load_dwordx4 v[42:45], v42, s[20:21]
	global_load_dwordx4 v[46:49], v46, s[20:21]
	global_load_dwordx4 v[50:53], v50, s[20:21]
	global_load_dwordx4 v[54:57], v54, s[20:21]
	global_load_dwordx4 v[58:61], v58, s[20:21]
	s_waitcnt vmcnt(6)
	v_pk_add_f16 v33, v33, v37
	v_pk_add_f16 v32, v32, v36
	v_pk_add_f16 v31, v31, v35
	v_pk_add_f16 v30, v30, v34
	s_waitcnt vmcnt(4)
	v_pk_add_f16 v34, v41, v45
	v_pk_add_f16 v35, v40, v44
	v_pk_add_f16 v36, v39, v43
	v_pk_add_f16 v37, v38, v42
	s_waitcnt vmcnt(2)
	v_pk_add_f16 v38, v49, v53
	v_pk_add_f16 v39, v48, v52
	v_pk_add_f16 v40, v47, v51
	v_pk_add_f16 v41, v46, v50
	s_waitcnt vmcnt(0)
	v_pk_add_f16 v42, v57, v61
	v_pk_add_f16 v43, v56, v60
	v_pk_add_f16 v44, v55, v59
	v_pk_add_f16 v45, v54, v58
	v_pk_add_f16 v30, v30, v37
	v_pk_add_f16 v31, v31, v36
	v_pk_add_f16 v32, v32, v35
	v_pk_add_f16 v33, v33, v34
	v_pk_add_f16 v34, v41, v45
	v_pk_add_f16 v35, v40, v44
	v_pk_add_f16 v36, v39, v43
	v_pk_add_f16 v37, v38, v42
	v_pk_add_f16 v36, v32, v36
	v_pk_add_f16 v37, v33, v37
	v_pk_add_f16 v33, v31, v35
	v_pk_add_f16 v31, v30, v34
	v_cvt_f32_f16_e32 v32, v33
	v_cvt_f32_f16_e32 v30, v31
	v_cvt_f32_f16_sdwa v31, v31 dst_sel:DWORD dst_unused:UNUSED_PAD src0_sel:WORD_1
	v_cvt_f32_f16_sdwa v33, v33 dst_sel:DWORD dst_unused:UNUSED_PAD src0_sel:WORD_1
	v_cvt_f32_f16_e32 v34, v36
	v_cvt_f32_f16_sdwa v35, v36 dst_sel:DWORD dst_unused:UNUSED_PAD src0_sel:WORD_1
	v_cvt_f32_f16_e32 v36, v37
	v_cvt_f32_f16_sdwa v37, v37 dst_sel:DWORD dst_unused:UNUSED_PAD src0_sel:WORD_1
	v_pk_add_f32 v[18:19], v[18:19], v[30:31]
	v_pk_add_f32 v[16:17], v[16:17], v[32:33]
	v_pk_add_f32 v[14:15], v[14:15], v[34:35]
	v_pk_add_f32 v[12:13], v[12:13], v[36:37]
	s_andn2_b64 exec, exec, s[30:31]
	s_cbranch_execnz .LBB3_4
	s_branch .Lagg_loop_done
.Lagg_n1:
	global_load_dword v30, v[2:3], off
	s_waitcnt vmcnt(0)
	v_mad_u32_u16 v39, v30, s34, v6
	global_load_dwordx4 v[30:33], v39, s[20:21]
	s_waitcnt vmcnt(0)
	v_cvt_f32_f16_e32 v34, v30
	v_cvt_f32_f16_sdwa v35, v30 dst_sel:DWORD dst_unused:UNUSED_PAD src0_sel:WORD_1
	v_cvt_f32_f16_e32 v36, v31
	v_cvt_f32_f16_sdwa v37, v31 dst_sel:DWORD dst_unused:UNUSED_PAD src0_sel:WORD_1
	v_cvt_f32_f16_e32 v38, v32
	v_cvt_f32_f16_sdwa v39, v32 dst_sel:DWORD dst_unused:UNUSED_PAD src0_sel:WORD_1
	v_cvt_f32_f16_e32 v40, v33
	v_cvt_f32_f16_sdwa v41, v33 dst_sel:DWORD dst_unused:UNUSED_PAD src0_sel:WORD_1
	v_pk_add_f32 v[18:19], v[18:19], v[34:35]
	v_pk_add_f32 v[16:17], v[16:17], v[36:37]
	v_pk_add_f32 v[14:15], v[14:15], v[38:39]
	v_pk_add_f32 v[12:13], v[12:13], v[40:41]
	s_branch .Lagg_loop_done
.Lagg_n2:
	global_load_dword v30, v[2:3], off
	s_waitcnt vmcnt(0)
	v_mad_u32_u16 v39, v30, s34, v6
	v_mad_u32_u16 v38, v30, s34, v6 op_sel:[1,0,0,0]
	global_load_dwordx4 v[30:33], v39, s[20:21]
	global_load_dwordx4 v[34:37], v38, s[20:21]
	s_waitcnt vmcnt(0)
	v_pk_add_f16 v33, v33, v37
	v_pk_add_f16 v32, v32, v36
	v_pk_add_f16 v31, v31, v35
	v_pk_add_f16 v30, v30, v34
	v_cvt_f32_f16_e32 v34, v30
	v_cvt_f32_f16_sdwa v35, v30 dst_sel:DWORD dst_unused:UNUSED_PAD src0_sel:WORD_1
	v_cvt_f32_f16_e32 v36, v31
	v_cvt_f32_f16_sdwa v37, v31 dst_sel:DWORD dst_unused:UNUSED_PAD src0_sel:WORD_1
	v_cvt_f32_f16_e32 v38, v32
	v_cvt_f32_f16_sdwa v39, v32 dst_sel:DWORD dst_unused:UNUSED_PAD src0_sel:WORD_1
	v_cvt_f32_f16_e32 v40, v33
	v_cvt_f32_f16_sdwa v41, v33 dst_sel:DWORD dst_unused:UNUSED_PAD src0_sel:WORD_1
	v_pk_add_f32 v[18:19], v[18:19], v[34:35]
	v_pk_add_f32 v[16:17], v[16:17], v[36:37]
	v_pk_add_f32 v[14:15], v[14:15], v[38:39]
	v_pk_add_f32 v[12:13], v[12:13], v[40:41]
	s_branch .Lagg_loop_done
.Lagg_n3:
	global_load_dwordx2 v[30:31], v[2:3], off
	s_waitcnt vmcnt(0)
	v_mad_u32_u16 v39, v30, s34, v6
	v_mad_u32_u16 v38, v30, s34, v6 op_sel:[1,0,0,0]
	v_mad_u32_u16 v40, v31, s34, v6
	global_load_dwordx4 v[30:33], v39, s[20:21]
	global_load_dwordx4 v[34:37], v38, s[20:21]
	global_load_dwordx4 v[38:41], v40, s[20:21]
	s_waitcnt vmcnt(1)
	v_pk_add_f16 v33, v33, v37
	v_pk_add_f16 v32, v32, v36
	v_pk_add_f16 v31, v31, v35
	v_pk_add_f16 v30, v30, v34
	s_waitcnt vmcnt(0)
	v_pk_add_f16 v30, v30, v38
	v_pk_add_f16 v31, v31, v39
	v_pk_add_f16 v32, v32, v40
	v_pk_add_f16 v33, v33, v41
	v_cvt_f32_f16_e32 v34, v30
	v_cvt_f32_f16_sdwa v35, v30 dst_sel:DWORD dst_unused:UNUSED_PAD src0_sel:WORD_1
	v_cvt_f32_f16_e32 v36, v31
	v_cvt_f32_f16_sdwa v37, v31 dst_sel:DWORD dst_unused:UNUSED_PAD src0_sel:WORD_1
	v_cvt_f32_f16_e32 v38, v32
	v_cvt_f32_f16_sdwa v39, v32 dst_sel:DWORD dst_unused:UNUSED_PAD src0_sel:WORD_1
	v_cvt_f32_f16_e32 v40, v33
	v_cvt_f32_f16_sdwa v41, v33 dst_sel:DWORD dst_unused:UNUSED_PAD src0_sel:WORD_1
	v_pk_add_f32 v[18:19], v[18:19], v[34:35]
	v_pk_add_f32 v[16:17], v[16:17], v[36:37]
	v_pk_add_f32 v[14:15], v[14:15], v[38:39]
	v_pk_add_f32 v[12:13], v[12:13], v[40:41]
	s_branch .Lagg_loop_done
.Lagg_n4:
	global_load_dwordx2 v[30:31], v[2:3], off
	s_waitcnt vmcnt(0)
	v_mad_u32_u16 v39, v30, s34, v6
	v_mad_u32_u16 v38, v30, s34, v6 op_sel:[1,0,0,0]
	v_mad_u32_u16 v40, v31, s34, v6
	v_mad_u32_u16 v42, v31, s34, v6 op_sel:[1,0,0,0]
	global_load_dwordx4 v[30:33], v39, s[20:21]
	global_load_dwordx4 v[34:37], v38, s[20:21]
	global_load_dwordx4 v[38:41], v40, s[20:21]
	global_load_dwordx4 v[42:45], v42, s[20:21]
	s_waitcnt vmcnt(2)
	v_pk_add_f16 v33, v33, v37
	v_pk_add_f16 v32, v32, v36
	v_pk_add_f16 v31, v31, v35
	v_pk_add_f16 v30, v30, v34
	s_waitcnt vmcnt(0)
	v_pk_add_f16 v34, v41, v45
	v_pk_add_f16 v35, v40, v44
	v_pk_add_f16 v36, v39, v43
	v_pk_add_f16 v37, v38, v42
	v_pk_add_f16 v30, v30, v37
	v_pk_add_f16 v31, v31, v36
	v_pk_add_f16 v32, v32, v35
	v_pk_add_f16 v33, v33, v34
	v_cvt_f32_f16_e32 v34, v30
	v_cvt_f32_f16_sdwa v35, v30 dst_sel:DWORD dst_unused:UNUSED_PAD src0_sel:WORD_1
	v_cvt_f32_f16_e32 v36, v31
	v_cvt_f32_f16_sdwa v37, v31 dst_sel:DWORD dst_unused:UNUSED_PAD src0_sel:WORD_1
	v_cvt_f32_f16_e32 v38, v32
	v_cvt_f32_f16_sdwa v39, v32 dst_sel:DWORD dst_unused:UNUSED_PAD src0_sel:WORD_1
	v_cvt_f32_f16_e32 v40, v33
	v_cvt_f32_f16_sdwa v41, v33 dst_sel:DWORD dst_unused:UNUSED_PAD src0_sel:WORD_1
	v_pk_add_f32 v[18:19], v[18:19], v[34:35]
	v_pk_add_f32 v[16:17], v[16:17], v[36:37]
	v_pk_add_f32 v[14:15], v[14:15], v[38:39]
	v_pk_add_f32 v[12:13], v[12:13], v[40:41]
	s_branch .Lagg_loop_done
.Lagg_n5:
	global_load_dwordx3 v[30:32], v[2:3], off
	s_waitcnt vmcnt(0)
	v_mad_u32_u16 v39, v30, s34, v6
	v_mad_u32_u16 v38, v30, s34, v6 op_sel:[1,0,0,0]
	v_mad_u32_u16 v40, v31, s34, v6
	v_mad_u32_u16 v42, v31, s34, v6 op_sel:[1,0,0,0]
	v_mad_u32_u16 v46, v32, s34, v6
	global_load_dwordx4 v[30:33], v39, s[20:21]
	global_load_dwordx4 v[34:37], v38, s[20:21]
	global_load_dwordx4 v[38:41], v40, s[20:21]
	global_load_dwordx4 v[42:45], v42, s[20:21]
	global_load_dwordx4 v[46:49], v46, s[20:21]
	s_waitcnt vmcnt(3)
	v_pk_add_f16 v33, v33, v37
	v_pk_add_f16 v32, v32, v36
	v_pk_add_f16 v31, v31, v35
	v_pk_add_f16 v30, v30, v34
	s_waitcnt vmcnt(1)
	v_pk_add_f16 v34, v41, v45
	v_pk_add_f16 v35, v40, v44
	v_pk_add_f16 v36, v39, v43
	v_pk_add_f16 v37, v38, v42
	v_pk_add_f16 v30, v30, v37
	v_pk_add_f16 v31, v31, v36
	v_pk_add_f16 v32, v32, v35
	v_pk_add_f16 v33, v33, v34
	s_waitcnt vmcnt(0)
	v_pk_add_f16 v30, v30, v46
	v_pk_add_f16 v31, v31, v47
	v_pk_add_f16 v32, v32, v48
	v_pk_add_f16 v33, v33, v49
	v_cvt_f32_f16_e32 v34, v30
	v_cvt_f32_f16_sdwa v35, v30 dst_sel:DWORD dst_unused:UNUSED_PAD src0_sel:WORD_1
	v_cvt_f32_f16_e32 v36, v31
	v_cvt_f32_f16_sdwa v37, v31 dst_sel:DWORD dst_unused:UNUSED_PAD src0_sel:WORD_1
	v_cvt_f32_f16_e32 v38, v32
	v_cvt_f32_f16_sdwa v39, v32 dst_sel:DWORD dst_unused:UNUSED_PAD src0_sel:WORD_1
	v_cvt_f32_f16_e32 v40, v33
	v_cvt_f32_f16_sdwa v41, v33 dst_sel:DWORD dst_unused:UNUSED_PAD src0_sel:WORD_1
	v_pk_add_f32 v[18:19], v[18:19], v[34:35]
	v_pk_add_f32 v[16:17], v[16:17], v[36:37]
	v_pk_add_f32 v[14:15], v[14:15], v[38:39]
	v_pk_add_f32 v[12:13], v[12:13], v[40:41]
	s_branch .Lagg_loop_done
.Lagg_n6:
	global_load_dwordx3 v[30:32], v[2:3], off
	s_waitcnt vmcnt(0)
	v_mad_u32_u16 v39, v30, s34, v6
	v_mad_u32_u16 v38, v30, s34, v6 op_sel:[1,0,0,0]
	v_mad_u32_u16 v40, v31, s34, v6
	v_mad_u32_u16 v42, v31, s34, v6 op_sel:[1,0,0,0]
	v_mad_u32_u16 v46, v32, s34, v6
	v_mad_u32_u16 v50, v32, s34, v6 op_sel:[1,0,0,0]
	global_load_dwordx4 v[30:33], v39, s[20:21]
	global_load_dwordx4 v[34:37], v38, s[20:21]
	global_load_dwordx4 v[38:41], v40, s[20:21]
	global_load_dwordx4 v[42:45], v42, s[20:21]
	global_load_dwordx4 v[46:49], v46, s[20:21]
	global_load_dwordx4 v[50:53], v50, s[20:21]
	s_waitcnt vmcnt(4)
	v_pk_add_f16 v33, v33, v37
	v_pk_add_f16 v32, v32, v36
	v_pk_add_f16 v31, v31, v35
	v_pk_add_f16 v30, v30, v34
	s_waitcnt vmcnt(2)
	v_pk_add_f16 v34, v41, v45
	v_pk_add_f16 v35, v40, v44
	v_pk_add_f16 v36, v39, v43
	v_pk_add_f16 v37, v38, v42
	v_pk_add_f16 v30, v30, v37
	v_pk_add_f16 v31, v31, v36
	v_pk_add_f16 v32, v32, v35
	v_pk_add_f16 v33, v33, v34
	s_waitcnt vmcnt(0)
	v_pk_add_f16 v38, v49, v53
	v_pk_add_f16 v39, v48, v52
	v_pk_add_f16 v40, v47, v51
	v_pk_add_f16 v41, v46, v50
	v_pk_add_f16 v30, v30, v41
	v_pk_add_f16 v31, v31, v40
	v_pk_add_f16 v32, v32, v39
	v_pk_add_f16 v33, v33, v38
	v_cvt_f32_f16_e32 v34, v30
	v_cvt_f32_f16_sdwa v35, v30 dst_sel:DWORD dst_unused:UNUSED_PAD src0_sel:WORD_1
	v_cvt_f32_f16_e32 v36, v31
	v_cvt_f32_f16_sdwa v37, v31 dst_sel:DWORD dst_unused:UNUSED_PAD src0_sel:WORD_1
	v_cvt_f32_f16_e32 v38, v32
	v_cvt_f32_f16_sdwa v39, v32 dst_sel:DWORD dst_unused:UNUSED_PAD src0_sel:WORD_1
	v_cvt_f32_f16_e32 v40, v33
	v_cvt_f32_f16_sdwa v41, v33 dst_sel:DWORD dst_unused:UNUSED_PAD src0_sel:WORD_1
	v_pk_add_f32 v[18:19], v[18:19], v[34:35]
	v_pk_add_f32 v[16:17], v[16:17], v[36:37]
	v_pk_add_f32 v[14:15], v[14:15], v[38:39]
	v_pk_add_f32 v[12:13], v[12:13], v[40:41]
	s_branch .Lagg_loop_done
.Lagg_n7:
	global_load_dwordx4 v[30:33], v[2:3], off
	s_waitcnt vmcnt(0)
	v_mad_u32_u16 v39, v30, s34, v6
	v_mad_u32_u16 v38, v30, s34, v6 op_sel:[1,0,0,0]
	v_mad_u32_u16 v40, v31, s34, v6
	v_mad_u32_u16 v42, v31, s34, v6 op_sel:[1,0,0,0]
	v_mad_u32_u16 v46, v32, s34, v6
	v_mad_u32_u16 v50, v32, s34, v6 op_sel:[1,0,0,0]
	v_mad_u32_u16 v54, v33, s34, v6
	global_load_dwordx4 v[30:33], v39, s[20:21]
	global_load_dwordx4 v[34:37], v38, s[20:21]
	global_load_dwordx4 v[38:41], v40, s[20:21]
	global_load_dwordx4 v[42:45], v42, s[20:21]
	global_load_dwordx4 v[46:49], v46, s[20:21]
	global_load_dwordx4 v[50:53], v50, s[20:21]
	global_load_dwordx4 v[54:57], v54, s[20:21]
	s_waitcnt vmcnt(5)
	v_pk_add_f16 v33, v33, v37
	v_pk_add_f16 v32, v32, v36
	v_pk_add_f16 v31, v31, v35
	v_pk_add_f16 v30, v30, v34
	s_waitcnt vmcnt(3)
	v_pk_add_f16 v34, v41, v45
	v_pk_add_f16 v35, v40, v44
	v_pk_add_f16 v36, v39, v43
	v_pk_add_f16 v37, v38, v42
	v_pk_add_f16 v30, v30, v37
	v_pk_add_f16 v31, v31, v36
	v_pk_add_f16 v32, v32, v35
	v_pk_add_f16 v33, v33, v34
	s_waitcnt vmcnt(1)
	v_pk_add_f16 v38, v49, v53
	v_pk_add_f16 v39, v48, v52
	v_pk_add_f16 v40, v47, v51
	v_pk_add_f16 v41, v46, v50
	s_waitcnt vmcnt(0)
	v_pk_add_f16 v41, v41, v54
	v_pk_add_f16 v40, v40, v55
	v_pk_add_f16 v39, v39, v56
	v_pk_add_f16 v38, v38, v57
	v_pk_add_f16 v30, v30, v41
	v_pk_add_f16 v31, v31, v40
	v_pk_add_f16 v32, v32, v39
	v_pk_add_f16 v33, v33, v38
	v_cvt_f32_f16_e32 v34, v30
	v_cvt_f32_f16_sdwa v35, v30 dst_sel:DWORD dst_unused:UNUSED_PAD src0_sel:WORD_1
	v_cvt_f32_f16_e32 v36, v31
	v_cvt_f32_f16_sdwa v37, v31 dst_sel:DWORD dst_unused:UNUSED_PAD src0_sel:WORD_1
	v_cvt_f32_f16_e32 v38, v32
	v_cvt_f32_f16_sdwa v39, v32 dst_sel:DWORD dst_unused:UNUSED_PAD src0_sel:WORD_1
	v_cvt_f32_f16_e32 v40, v33
	v_cvt_f32_f16_sdwa v41, v33 dst_sel:DWORD dst_unused:UNUSED_PAD src0_sel:WORD_1
	v_pk_add_f32 v[18:19], v[18:19], v[34:35]
	v_pk_add_f32 v[16:17], v[16:17], v[36:37]
	v_pk_add_f32 v[14:15], v[14:15], v[38:39]
	v_pk_add_f32 v[12:13], v[12:13], v[40:41]
	s_branch .Lagg_loop_done
